# B1': grid barrier release - the last XCD leader bumps sixteen per-XCC release words (128 B apart, next to TOPGEN) and each XCC's waiting workgroups poll their own word (32 pollers per line, not 256);
# speedup vs baseline: 1.0022x; 1.0018x over previous
.LBB0_165:
	s_or_b64 exec, exec, s[8:9]
	v_cvt_f32_u32_e32 v4, v2
	s_waitcnt vmcnt(0)
	v_readfirstlane_b32 s6, v3
	v_sub_u32_e32 v3, 0, v2
	v_rcp_iflag_f32_e32 v4, v4
	v_add_u32_e32 v5, s6, v1
	v_mul_f32_e32 v4, 0x4f7ffffe, v4
	v_cvt_u32_f32_e32 v4, v4
	v_mul_lo_u32 v1, v3, v4
	v_mul_hi_u32 v1, v4, v1
	v_add_u32_e32 v1, v4, v1
	v_mul_hi_u32 v1, v5, v1
	v_mul_lo_u32 v3, v1, v2
	v_sub_u32_e32 v3, v5, v3
	v_add_u32_e32 v4, 1, v1
	v_cmp_ge_u32_e32 vcc, v3, v2
	s_nop 1
	v_cndmask_b32_e32 v1, v1, v4, vcc
	v_sub_u32_e32 v4, v3, v2
	v_cndmask_b32_e32 v3, v3, v4, vcc
	v_add_u32_e32 v4, 1, v1
	v_cmp_ge_u32_e32 vcc, v3, v2
	v_add_u32_e32 v3, 1, v5
	s_nop 0
	v_cndmask_b32_e32 v1, v1, v4, vcc
	v_mul_lo_u32 v4, v2, v1
	v_add_u32_e32 v2, v4, v2
	v_cmp_ne_u32_e32 vcc, v3, v2
	s_and_saveexec_b64 s[6:7], vcc
	s_xor_b64 s[6:7], exec, s[6:7]
	s_cbranch_execz .LBB0_179
	s_waitcnt lgkmcnt(0)
	v_mov_b32_e32 v0, 0
	s_sub_u32 s12, s4, s2
	s_lshr_b32 s12, s12, 1
	s_add_u32 s12, s12, s2
	s_addc_u32 s13, s3, 0
	s_add_u32 s12, s12, 0xb580
	s_addc_u32 s13, s13, 0
	global_load_dword v0, v0, s[12:13] sc1
	s_waitcnt vmcnt(0)
	v_cmp_eq_u32_e32 vcc, v0, v1
	s_and_saveexec_b64 s[8:9], vcc
	s_cbranch_execz .LBB0_178
	s_add_u32 s10, s2, 0x10200
	s_addc_u32 s11, s3, 0
	s_mov_b32 s24, 1
	s_mov_b64 s[14:15], 0
	v_mov_b32_e32 v0, 0
	s_branch .LBB0_169

.LBB0_194:
	s_or_b64 exec, exec, s[6:7]
	s_and_saveexec_b64 s[2:3], s[10:11]
	s_cbranch_execz .LBB0_196
	v_mov_b32_e32 v2, 1
	global_atomic_add v[0:1], v2, off
	global_atomic_add v[0:1], v2, off offset:128
	global_atomic_add v[0:1], v2, off offset:256
	global_atomic_add v[0:1], v2, off offset:384
	global_atomic_add v[0:1], v2, off offset:512
	global_atomic_add v[0:1], v2, off offset:640
	global_atomic_add v[0:1], v2, off offset:768
	global_atomic_add v[0:1], v2, off offset:896
	global_atomic_add v[0:1], v2, off offset:1024
	global_atomic_add v[0:1], v2, off offset:1152
	global_atomic_add v[0:1], v2, off offset:1280
	global_atomic_add v[0:1], v2, off offset:1408
	global_atomic_add v[0:1], v2, off offset:1536
	global_atomic_add v[0:1], v2, off offset:1664
	global_atomic_add v[0:1], v2, off offset:1792
	global_atomic_add v[0:1], v2, off offset:1920
	global_atomic_add v[0:1], v2, off offset:2048

.LBB0_220:
	s_or_b64 exec, exec, s[8:9]
	v_cvt_f32_u32_e32 v4, v2
	s_waitcnt vmcnt(0)
	v_readfirstlane_b32 s6, v3
	v_sub_u32_e32 v3, 0, v2
	v_rcp_iflag_f32_e32 v4, v4
	v_add_u32_e32 v5, s6, v1
	v_mul_f32_e32 v4, 0x4f7ffffe, v4
	v_cvt_u32_f32_e32 v4, v4
	v_mul_lo_u32 v1, v3, v4
	v_mul_hi_u32 v1, v4, v1
	v_add_u32_e32 v1, v4, v1
	v_mul_hi_u32 v1, v5, v1
	v_mul_lo_u32 v3, v1, v2
	v_sub_u32_e32 v3, v5, v3
	v_add_u32_e32 v4, 1, v1
	v_cmp_ge_u32_e32 vcc, v3, v2
	s_nop 1
	v_cndmask_b32_e32 v1, v1, v4, vcc
	v_sub_u32_e32 v4, v3, v2
	v_cndmask_b32_e32 v3, v3, v4, vcc
	v_add_u32_e32 v4, 1, v1
	v_cmp_ge_u32_e32 vcc, v3, v2
	v_add_u32_e32 v3, 1, v5
	s_nop 0
	v_cndmask_b32_e32 v1, v1, v4, vcc
	v_mul_lo_u32 v4, v2, v1
	v_add_u32_e32 v2, v4, v2
	v_cmp_ne_u32_e32 vcc, v3, v2
	s_and_saveexec_b64 s[6:7], vcc
	s_xor_b64 s[6:7], exec, s[6:7]
	s_cbranch_execz .LBB0_234
	s_waitcnt lgkmcnt(0)
	v_mov_b32_e32 v0, 0
	s_sub_u32 s12, s4, s0
	s_lshr_b32 s12, s12, 1
	s_add_u32 s12, s12, s0
	s_addc_u32 s13, s1, 0
	s_add_u32 s12, s12, 0xb580
	s_addc_u32 s13, s13, 0
	global_load_dword v0, v0, s[12:13] sc1
	s_waitcnt vmcnt(0)
	v_cmp_eq_u32_e32 vcc, v0, v1
	s_and_saveexec_b64 s[8:9], vcc
	s_cbranch_execz .LBB0_233
	s_add_u32 s10, s0, 0x10200
	s_addc_u32 s11, s1, 0
	s_mov_b32 s24, 1
	s_mov_b64 s[14:15], 0
	v_mov_b32_e32 v0, 0
	s_branch .LBB0_224

.LBB0_249:
	s_or_b64 exec, exec, s[6:7]
	s_and_saveexec_b64 s[0:1], s[10:11]
	s_cbranch_execz .LBB0_251
	v_mov_b32_e32 v2, 1
	global_atomic_add v[0:1], v2, off
	global_atomic_add v[0:1], v2, off offset:128
	global_atomic_add v[0:1], v2, off offset:256
	global_atomic_add v[0:1], v2, off offset:384
	global_atomic_add v[0:1], v2, off offset:512
	global_atomic_add v[0:1], v2, off offset:640
	global_atomic_add v[0:1], v2, off offset:768
	global_atomic_add v[0:1], v2, off offset:896
	global_atomic_add v[0:1], v2, off offset:1024
	global_atomic_add v[0:1], v2, off offset:1152
	global_atomic_add v[0:1], v2, off offset:1280
	global_atomic_add v[0:1], v2, off offset:1408
	global_atomic_add v[0:1], v2, off offset:1536
	global_atomic_add v[0:1], v2, off offset:1664
	global_atomic_add v[0:1], v2, off offset:1792
	global_atomic_add v[0:1], v2, off offset:1920
	global_atomic_add v[0:1], v2, off offset:2048

.LBB0_292:
	s_or_b64 exec, exec, s[8:9]
	v_cvt_f32_u32_e32 v4, v2
	s_waitcnt vmcnt(0)
	v_readfirstlane_b32 s6, v3
	v_sub_u32_e32 v3, 0, v2
	v_rcp_iflag_f32_e32 v4, v4
	v_add_u32_e32 v5, s6, v1
	v_mul_f32_e32 v4, 0x4f7ffffe, v4
	v_cvt_u32_f32_e32 v4, v4
	v_mul_lo_u32 v1, v3, v4
	v_mul_hi_u32 v1, v4, v1
	v_add_u32_e32 v1, v4, v1
	v_mul_hi_u32 v1, v5, v1
	v_mul_lo_u32 v3, v1, v2
	v_sub_u32_e32 v3, v5, v3
	v_add_u32_e32 v4, 1, v1
	v_cmp_ge_u32_e32 vcc, v3, v2
	s_nop 1
	v_cndmask_b32_e32 v1, v1, v4, vcc
	v_sub_u32_e32 v4, v3, v2
	v_cndmask_b32_e32 v3, v3, v4, vcc
	v_add_u32_e32 v4, 1, v1
	v_cmp_ge_u32_e32 vcc, v3, v2
	v_add_u32_e32 v3, 1, v5
	s_nop 0
	v_cndmask_b32_e32 v1, v1, v4, vcc
	v_mul_lo_u32 v4, v2, v1
	v_add_u32_e32 v2, v4, v2
	v_cmp_ne_u32_e32 vcc, v3, v2
	s_and_saveexec_b64 s[6:7], vcc
	s_xor_b64 s[6:7], exec, s[6:7]
	s_cbranch_execz .LBB0_306
	s_waitcnt lgkmcnt(0)
	s_sub_u32 s12, s4, s2
	s_lshr_b32 s12, s12, 1
	s_add_u32 s12, s12, s2
	s_addc_u32 s13, s3, 0
	s_add_u32 s12, s12, 0xb580
	s_addc_u32 s13, s13, 0
	global_load_dword v0, v169, s[12:13] sc1
	s_waitcnt vmcnt(0)
	v_cmp_eq_u32_e32 vcc, v0, v1
	s_and_saveexec_b64 s[8:9], vcc
	s_cbranch_execz .LBB0_305
	s_add_u32 s10, s2, 0x10200
	s_addc_u32 s11, s3, 0
	s_mov_b32 s24, 1
	s_mov_b64 s[14:15], 0
	s_branch .LBB0_296

.LBB0_321:
	s_or_b64 exec, exec, s[8:9]
	s_and_saveexec_b64 s[2:3], s[10:11]
	s_cbranch_execz .LBB0_323
	global_atomic_add v[0:1], v190, off
	global_atomic_add v[0:1], v190, off offset:128
	global_atomic_add v[0:1], v190, off offset:256
	global_atomic_add v[0:1], v190, off offset:384
	global_atomic_add v[0:1], v190, off offset:512
	global_atomic_add v[0:1], v190, off offset:640
	global_atomic_add v[0:1], v190, off offset:768
	global_atomic_add v[0:1], v190, off offset:896
	global_atomic_add v[0:1], v190, off offset:1024
	global_atomic_add v[0:1], v190, off offset:1152
	global_atomic_add v[0:1], v190, off offset:1280
	global_atomic_add v[0:1], v190, off offset:1408
	global_atomic_add v[0:1], v190, off offset:1536
	global_atomic_add v[0:1], v190, off offset:1664
	global_atomic_add v[0:1], v190, off offset:1792
	global_atomic_add v[0:1], v190, off offset:1920
	global_atomic_add v[0:1], v190, off offset:2048
